# P7: per-thread gather-index LDS addresses precomputed once per phase; the last-iteration recompute is two LDS reads and four adds
# speedup vs baseline: 1.0162x; 1.0153x over previous
; template <class Epi, class Sched>
; __device__ __forceinline__ void gemm_phase(LAS unsigned char* lds, const Sched& S, const Epi& E) {
;     ...
;                 for (int i = 0; i < 2; ++i) { int R, C; stage_rc(tz * 16 + i * 8192, R, C);
; #pragma unroll
;                     for (int h = 0; h < 2; ++h) vA[h][i] = (unsigned)(lidx[h * HALF + R] * RP + C * 2); } } }
.LBB0_724:
	s_add_u32 s12, s88, 0x3a800000
	s_addc_u32 s13, s89, 0
	s_lshl_b32 s2, s2, 12
	s_addk_i32 s7, 0x80
	s_lshl_b32 s14, s3, 13
	s_and_b32 s15, s2, 0x3000
	s_and_b32 s7, s7, 0x780
	s_add_u32 s2, s28, s7
	v_mov_b32_e32 v2, v1
	s_waitcnt vmcnt(2)
	s_barrier
	s_addc_u32 s3, s29, 0
	s_add_i32 m0, s39, 0x18000
	v_lshlrev_b32_e32 v3, 6, v0
	global_load_lds_dwordx4 v2, s[2:3]
	v_mov_b32_e32 v2, v190
	s_add_i32 m0, s39, 0x1a000
	v_lshlrev_b32_e32 v5, 2, v0
	global_load_lds_dwordx4 v2, s[2:3]
	s_add_u32 s2, s58, s7
	s_addc_u32 s3, s59, 0
	v_mov_b32_e32 v2, v192
	s_add_i32 s70, s39, 0x8000
	s_mov_b32 m0, s70
	s_add_i32 s71, s39, 0xa000
	global_load_lds_dwordx4 v2, s[2:3]
	v_mov_b32_e32 v2, v194
	s_mov_b32 m0, s71
	v_and_b32_e32 v3, 0x3c0, v3
	global_load_lds_dwordx4 v2, s[2:3]
	s_add_u32 s2, s4, s7
	v_mov_b32_e32 v2, v1
	s_addc_u32 s3, s5, 0
	s_add_i32 m0, s39, 0x1c000
	v_and_b32_e32 v6, 32, v5
	global_load_lds_dwordx4 v2, s[2:3]
	v_mov_b32_e32 v2, v190
	s_add_i32 m0, s39, 0x1e000
	s_cmpk_lt_u32 s6, 0x100
	global_load_lds_dwordx4 v2, s[2:3]
	v_and_b32_e32 v2, 48, v0
	v_or_b32_e32 v4, v3, v2
	v_bitop3_b32 v2, v3, v6, v2 bitop3:0x36
	v_bitop3_b32 v3, s14, v4, v6 bitop3:0xf6
	v_or_b32_e32 v196, s15, v2
	s_cselect_b64 s[14:15], -1, 0
	s_add_i32 s3, 0, 0x27d04
	v_writelane_b32 v255, s3, 55
	s_add_i32 s3, 0, 0x27d4c
	v_writelane_b32 v255, s3, 56
	s_add_i32 s3, 0, 0x27d54
	v_writelane_b32 v255, s3, 57
	s_add_i32 s3, 0, 0x27d5c
	v_writelane_b32 v255, s3, 58
	s_add_i32 s3, 0, 0x27d64
	s_waitcnt vmcnt(0)
	v_writelane_b32 v255, s3, 59
	s_add_i32 s3, 0, 0x27d6c
	s_mov_b32 s4, 0
	s_add_i32 s2, 0, 0x27d80
	v_writelane_b32 v255, s3, 60
	s_add_i32 s3, 0, 0x27d74
	v_mov_b32_e32 v187, 0
	v_add_u32_e32 v197, s60, v5
	s_ashr_i32 s96, s96, 31
	s_add_i32 s9, 0, 0x27d0c
	s_add_i32 s8, 0, 0x27d14
	s_add_i32 s17, 0, 0x27d1c
	s_add_i32 s50, 0, 0x27d24
	s_add_i32 s10, 0, 0x27d2c
	s_add_i32 s11, 0, 0x27d34
	s_add_i32 s56, 0, 0x27d3c
	s_add_i32 s57, 0, 0x27d44
	v_writelane_b32 v255, s3, 61
	s_add_i32 s91, 0, 0x27d7c
	v_lshlrev_b32_e32 v198, 2, v0
	s_add_i32 s92, 0, 0x10000
	s_add_i32 s93, 0, 0x14000
	s_mov_b32 s5, s4
	s_mov_b32 s6, s4
	s_mov_b32 s7, s4
	s_mov_b32 s16, 0xc01d265f
	s_mov_b32 s94, 0xc0e00000
	v_mov_b32_e32 v199, s2
	v_add_u32_e32 v200, 0, v3
	v_mov_b32_e32 v201, 1
	v_mov_b32_e32 v42, 0xba1d265f
	v_mov_b32_e32 v46, 0x39800000
	v_mov_b32_e32 v202, 0x40e00000
	v_mov_b32_e32 v188, 0x3fd083aa
	s_mov_b32 s95, s4
	s_mov_b64 s[24:25], s[28:29]
	s_barrier
	v_mov_b32_e32 v4, v0
	s_nop 0
	v_ashrrev_i32_e32 v6, 31, v4
	v_lshrrev_b32_e32 v6, 26, v6
	v_lshlrev_b32_e32 v5, 4, v4
	v_add_u32_e32 v6, v4, v6
	v_bfe_i32 v4, v4, 27, 1
	v_lshrrev_b32_e32 v4, 22, v4
	v_add_u32_e32 v4, v5, v4
	v_and_b32_e32 v4, 0xfffffc00, v4
	v_sub_u32_e32 v4, v5, v4
	v_lshrrev_b32_e32 v7, 4, v4
	v_bitop3_b32 v4, v7, v4, 32 bitop3:0x6c
	v_ashrrev_i32_e32 v7, 31, v4
	v_lshrrev_b32_e32 v7, 26, v7
	v_ashrrev_i32_e32 v6, 6, v6
	v_add_u32_e32 v7, v4, v7
	v_ashrrev_i32_e32 v8, 6, v7
	v_lshlrev_b32_e32 v6, 5, v6
	v_and_b32_e32 v9, 32, v6
	v_and_b32_e32 v10, 0xc0, v7
	v_lshlrev_b32_e32 v7, 2, v8
	v_and_b32_e32 v6, 0xffffffc0, v6
	v_add3_u32 v6, s60, v7, v6
	v_mov_b32_e32 v246, v6
	v_sub_u32_e32 v4, v4, v10
	v_ashrrev_i16_sdwa v4, v201, sext(v4) dst_sel:DWORD dst_unused:UNUSED_PAD src0_sel:DWORD src1_sel:BYTE_0
	v_bfe_i32 v4, v4, 0, 16
	v_add_lshl_u32 v4, v9, v4, 1
	v_mov_b32_e32 v247, v4
	v_add_u32_e32 v4, 0x2000, v5
	v_ashrrev_i32_e32 v5, 31, v4
	v_lshrrev_b32_e32 v5, 22, v5
	v_add_u32_e32 v5, v4, v5
	v_ashrrev_i32_e32 v5, 10, v5
	v_mul_i32_i24_e32 v6, 0x400, v5
	v_sub_u32_e32 v4, v4, v6
	v_lshrrev_b32_e32 v6, 4, v4
	v_bitop3_b32 v4, v6, v4, 32 bitop3:0x6c
	v_ashrrev_i32_e32 v6, 31, v4
	v_lshrrev_b32_e32 v6, 26, v6
	v_add_u32_e32 v6, v4, v6
	v_ashrrev_i32_e32 v7, 6, v6
	v_lshlrev_b32_e32 v5, 5, v5
	v_and_b32_e32 v8, 32, v5
	v_and_b32_e32 v9, 0xc0, v6
	v_lshlrev_b32_e32 v6, 2, v7
	v_and_b32_e32 v5, 0xffffffc0, v5
	v_add3_u32 v5, s60, v6, v5
	v_mov_b32_e32 v248, v5
	v_sub_u32_e32 v4, v4, v9
	v_ashrrev_i16_sdwa v4, v201, sext(v4) dst_sel:DWORD dst_unused:UNUSED_PAD src0_sel:DWORD src1_sel:BYTE_0
	v_bfe_i32 v4, v4, 0, 16
	v_add_lshl_u32 v4, v8, v4, 1
	v_mov_b32_e32 v249, v4
	s_branch .LBB0_727

; #define PG8_STAGE(bufoff, gbase, voff) do { if constexpr (!(Sched::CRIP & 2)) _Pragma("unroll") for (int _i = 0; _i < 2; ++_i) { unsigned _o = (voff)[_i]; asm volatile("" : "+v"(_o)); \
;         __builtin_amdgcn_global_load_lds((const unsigned*)((const char*)(gbase) + _o), (LAS unsigned*)(lds + (bufoff) + ldsw + _i * 8192), 16, 0, 0); } } while (0)
; #define PG8_LDA(dst, b, h) do { if constexpr (!(Sched::CRIP & 4)) _Pragma("unroll") for (int m = 0; m < 4; ++m) dst[m] = PG8_CAT(*(const LAS i32x4*)(lds + PG8_SA(b, h) + aoff + m * 2048), *(const LAS i32x4*)(lds + PG8_SA(b, h) + aoff + m * 2048 + 1024)); } while (0)
; #define PG8_LDB(dst, b, h) do { if constexpr (!(Sched::CRIP & 4)) _Pragma("unroll") for (int n = 0; n < 2; ++n) dst[n] = PG8_CAT(*(const LAS i32x4*)(lds + PG8_SB(b, h) + boff + n * 2048), *(const LAS i32x4*)(lds + PG8_SB(b, h) + boff + n * 2048 + 1024)); } while (0)
; #define PG8_WAIT_V(n) asm volatile("s_waitcnt vmcnt(" #n ")" ::: "memory")
; #define PG8_WAIT_L(n) asm volatile("s_waitcnt lgkmcnt(" #n ")" ::: "memory")
; #define PG8_BAR __builtin_amdgcn_s_barrier()
; #define PG8_SCHED __builtin_amdgcn_sched_barrier(0)
; template <class Epi, class Sched>
; __device__ __forceinline__ void gemm_phase(LAS unsigned char* lds, const Sched& S, const Epi& E) {
;     ...
;             PG8_LDB(B0, 0, 0); PG8_LDB(B1, 0, 1); PG8_SCHED; PG8_LDA(At, 0, 0); PG8_STAGE(PG8_SA(1, 1), a1, vA[1]);
;             PG8_WAIT_V(8); PG8_WAIT_L(0); PG8_BAR; PG8_MMA(0, 0, At, B0); PG8_MMA(0, 1, At, B1); PG8_BAR2; PG8_SCHED;
;             if constexpr (Sched::GATHER) { if (last && has_next) {
;                 int tz = threadIdx.x; asm volatile("" : "+v"(tz));
; #pragma unroll
;                 for (int i = 0; i < 2; ++i) { int R, C; stage_rc(tz * 16 + i * 8192, R, C);
; #pragma unroll
;                     for (int h = 0; h < 2; ++h) vA[h][i] = (unsigned)(lidx[h * HALF + R] * RP + C * 2); } } }
.LBB0_735:
	v_add_u32_e32 v10, 0, v196
	v_add_u32_e32 v11, 0x10000, v10
	v_add_u32_e32 v30, 0x14000, v10
	ds_read_b128 v[2:5], v11
	ds_read_b128 v[6:9], v11 offset:1024
	ds_read_b128 v[18:21], v11 offset:2048
	ds_read_b128 v[22:25], v11 offset:3072
	ds_read_b128 v[10:13], v30
	ds_read_b128 v[14:17], v30 offset:1024
	ds_read_b128 v[26:29], v30 offset:2048
	ds_read_b128 v[30:33], v30 offset:3072
	s_cmp_eq_u32 s52, 12
	s_cselect_b64 s[34:35], -1, 0
	s_and_b32 s30, s21, 0x780
	s_add_u32 s30, s58, s30
	s_addc_u32 s31, s59, 0
	v_mov_b32_e32 v45, v193
	s_mov_b32 m0, s27
	ds_read_b128 v[204:207], v200
	ds_read_b128 v[208:211], v200 offset:1024
	ds_read_b128 v[214:217], v200 offset:2048
	ds_read_b128 v[218:221], v200 offset:3072
	ds_read_b128 v[222:225], v200 offset:4096
	ds_read_b128 v[226:229], v200 offset:5120
	ds_read_b128 v[230:233], v200 offset:6144
	ds_read_b128 v[234:237], v200 offset:7168
	s_nop 0
	global_load_lds_dwordx4 v45, s[30:31]
	v_mov_b32_e32 v45, v195
	s_mov_b32 m0, s62
	s_nop 0
	global_load_lds_dwordx4 v45, s[30:31]
	s_waitcnt vmcnt(8)
	s_waitcnt lgkmcnt(0)
	s_barrier
	s_setprio 1
	s_waitcnt lgkmcnt(0)
	s_nop 1
	v_mfma_scale_f32_16x16x128_f8f6f4 v[178:181], v[2:9], v[204:211], v[178:181], v191, v191 op_sel_hi:[0,0,0]
	v_mfma_scale_f32_16x16x128_f8f6f4 v[170:173], v[18:25], v[204:211], v[170:173], v191, v191 op_sel_hi:[0,0,0]
	v_mfma_scale_f32_16x16x128_f8f6f4 v[162:165], v[2:9], v[214:221], v[162:165], v191, v191 op_sel_hi:[0,0,0]
	v_mfma_scale_f32_16x16x128_f8f6f4 v[154:157], v[18:25], v[214:221], v[154:157], v191, v191 op_sel_hi:[0,0,0]
	v_mfma_scale_f32_16x16x128_f8f6f4 v[146:149], v[2:9], v[222:229], v[146:149], v191, v191 op_sel_hi:[0,0,0]
	v_mfma_scale_f32_16x16x128_f8f6f4 v[138:141], v[18:25], v[222:229], v[138:141], v191, v191 op_sel_hi:[0,0,0]
	v_mfma_scale_f32_16x16x128_f8f6f4 v[130:133], v[2:9], v[230:237], v[130:133], v191, v191 op_sel_hi:[0,0,0]
	v_mfma_scale_f32_16x16x128_f8f6f4 v[122:125], v[18:25], v[230:237], v[122:125], v191, v191 op_sel_hi:[0,0,0]
	s_setprio 0
	s_setprio 1
	s_nop 1
	v_mfma_scale_f32_16x16x128_f8f6f4 v[182:185], v[10:17], v[204:211], v[182:185], v191, v191 op_sel_hi:[0,0,0]
	v_mfma_scale_f32_16x16x128_f8f6f4 v[174:177], v[26:33], v[204:211], v[174:177], v191, v191 op_sel_hi:[0,0,0]
	v_mfma_scale_f32_16x16x128_f8f6f4 v[166:169], v[10:17], v[214:221], v[166:169], v191, v191 op_sel_hi:[0,0,0]
	v_mfma_scale_f32_16x16x128_f8f6f4 v[158:161], v[26:33], v[214:221], v[158:161], v191, v191 op_sel_hi:[0,0,0]
	v_mfma_scale_f32_16x16x128_f8f6f4 v[150:153], v[10:17], v[222:229], v[150:153], v191, v191 op_sel_hi:[0,0,0]
	v_mfma_scale_f32_16x16x128_f8f6f4 v[142:145], v[26:33], v[222:229], v[142:145], v191, v191 op_sel_hi:[0,0,0]
	v_mfma_scale_f32_16x16x128_f8f6f4 v[134:137], v[10:17], v[230:237], v[134:137], v191, v191 op_sel_hi:[0,0,0]
	v_mfma_scale_f32_16x16x128_f8f6f4 v[126:129], v[26:33], v[230:237], v[126:129], v191, v191 op_sel_hi:[0,0,0]
	s_setprio 0
	s_barrier
	s_and_b64 s[30:31], s[2:3], s[34:35]
	s_andn2_b64 vcc, exec, s[30:31]
	s_cbranch_vccnz .LBB0_734
	ds_read2st64_b32 v[48:49], v246 offset1:2
	ds_read2st64_b32 v[250:251], v248 offset1:2
	s_waitcnt lgkmcnt(0)
	v_lshl_add_u32 v192, v48, 11, v247
	v_lshl_add_u32 v193, v49, 11, v247
	v_lshl_add_u32 v194, v250, 11, v249
	v_lshl_add_u32 v195, v251, 11, v249
	s_branch .LBB0_734
